# diff-attention loop: per-iteration 4-byte touches of the next iteration's K/V rows so the staging loads hit the XCD L2
# baseline (speedup 1.0000x reference)
.LBB0_1354:
	s_lshr_b32 s98, s64, 5
	s_and_b32 s99, s98, 1
	s_lshl_b32 s99, s99, 6
	s_add_i32 s99, s99, s85
	s_add_i32 s99, s99, 32
	v_add_u32_e32 v231, s99, v233
	v_mul_u32_u24_e32 v231, 0x3100, v231
	s_lshr_b32 s99, s98, 1
	s_lshl_b32 s99, s99, 7
	s_add_u32 s2, s80, s99
	s_addc_u32 s3, s81, 0
	global_load_dword v231, v231, s[2:3]
	s_cmp_ge_u32 s98, 4
	s_cbranch_scc1 .Lkvpf_0
	s_add_u32 s2, s78, s99
	s_addc_u32 s3, s79, 0
	global_load_dword v231, v231, s[2:3]
